# dilated units: accumulator / constant initialisation moved ahead of the tile wait and barrier (runs under the DMA latency)
# speedup vs baseline: 1.0090x; 1.0090x over previous
; #define ATT_WAIT_BAR(N) asm volatile("s_waitcnt vmcnt(" #N ") lgkmcnt(0)\n\ts_barrier" ::: "memory")
; #pragma unroll
;         for (int i = 0; i < 8; ++i) { const int r = 2 * i; kc[i] = (f32x2_t){sd * (float)((r & 3) + 8 * (r >> 2)), sd * (float)(((r + 1) & 3) + 8 * ((r + 1) >> 2))}; } }
;     __device__ __forceinline__ void init(f32x16& c0, f32x16& c1, int t) const {
;         const int dt = t - (w >> 1);
;         const float base = basel + (float)dt * d64;
; #pragma unroll
;         for (int i = 0; i < 8; ++i) { const f32x2_t p = kc[i] + base, q = p + d32; c0[2 * i] = p[0]; c0[2 * i + 1] = p[1]; c1[2 * i] = q[0]; c1[2 * i + 1] = q[1]; }
; template <class BIAS>
; __device__ __forceinline__ void attn_tiles(char* shm, const UnitIO& io, int t_begin, int t_end, const BIAS& B, int tid) {
;     ...
;     f32x16 o[2]; o[0] = f32x16{}; o[1] = f32x16{}; float l_reg = 0.f;
;     if (nt_ > 2) ATT_WAIT_BAR(4); else if (nt_ > 1) ATT_WAIT_BAR(2); else ATT_WAIT_BAR(0);
.Ldl_ret:
	v_readlane_b32 s62, v191, 0
	v_readlane_b32 s63, v191, 1
	v_readlane_b32 s64, v191, 2
	v_readlane_b32 s65, v191, 3
	v_readlane_b32 s66, v191, 4
	v_readlane_b32 s67, v191, 5
	v_readlane_b32 s75, v191, 6
	s_branch .Ldl_post2
.Ldl_post:
.Ldl_post2:
	v_mov_b32_e32 v190, v191
	v_mov_b32_e32 v2, 0
	v_mov_b32_e32 v16, v2
	v_mov_b32_e32 v17, v2
	v_mul_f32_e32 v156, 0x42000000, v155
	v_mov_b32_e32 v3, v2
	v_mov_b32_e32 v4, v2
	v_mov_b32_e32 v5, v2
	v_mov_b32_e32 v6, v2
	v_mov_b32_e32 v7, v2
	v_mov_b32_e32 v8, v2
	v_mov_b32_e32 v9, v2
	v_mov_b32_e32 v10, v2
	v_mov_b32_e32 v11, v2
	v_mov_b32_e32 v12, v2
	v_mov_b32_e32 v13, v2
	v_mov_b32_e32 v14, v2
	v_mov_b32_e32 v15, v2
	v_mov_b64_e32 v[32:33], v[16:17]
	v_mul_f32_e32 v149, 0x42800000, v155
	v_mul_f32_e32 v154, 0, v155
	v_writelane_b32 v254, s3, 10
	v_mul_f32_e32 v0, v155, v196
	v_mov_b32_e32 v176, v156
	v_mov_b32_e32 v177, v156
	v_mov_b64_e32 v[30:31], v[14:15]
	v_mov_b64_e32 v[28:29], v[12:13]
	v_mov_b64_e32 v[26:27], v[10:11]
	v_mov_b64_e32 v[24:25], v[8:9]
	v_mov_b64_e32 v[22:23], v[6:7]
	v_mov_b64_e32 v[20:21], v[4:5]
	v_mov_b64_e32 v[18:19], v[2:3]
	v_mov_b32_e32 v151, v2
	s_cmp_eq_u32 s100, 0
	s_cbranch_scc1 .Ldl_w5
	s_waitcnt vmcnt(0) lgkmcnt(0)
	s_branch .Ldl_wb
.Ldl_w5:
	s_waitcnt vmcnt(5) lgkmcnt(0)
.Ldl_wb:
	s_barrier
	s_branch .LBB0_365
